# v55 + the half-idle tail rounds' weight-conversion burst delayed by two s_sleep 100 (about 6 us), away from the working workgroups' unit ramp
# baseline (speedup 1.0000x reference)
; #define LAS __attribute__((address_space(3)))
; template <bool WT> __device__ __forceinline__ void convert_items(LAS unsigned char* lds, unsigned char* ws, const float* const* in, int l, int it0, int it1, int gw, int NGW, int wave, int lane_in) {
;     int lane = lane_in; asm volatile("" : "+v"(lane));
;     LAS float* scr = (LAS float*)(lds + RING_OFF + wave * 16384);
;     bf16* WL = (bf16*)(ws + WS_W) + (size_t)l * LAYER_W_ELEMS;
; #pragma unroll 1
;     for (int base = it0 + gw; base < it1; base += 3 * NGW) {
;         const int i1 = base + NGW, i2 = base + 2 * NGW; const bool h1 = i1 < it1, h2 = i2 < it1;
;         CvtItem a = cvt_decode(base, l, in, WL), b = cvt_decode(h1 ? i1 : base, l, in, WL), c = cvt_decode(h2 ? i2 : base, l, in, WL);
;         a.late = b.late = c.late = (!WT && l >= 1);
;         CvtLoad la, lb, lc;
;         cvt_load(a, lane, la); cvt_load(b, lane, lb); cvt_load(c, lane, lc);
;         cvt_process<WT>(a, la, scr, lane);
;         if (h1) cvt_process<WT>(b, lb, scr, lane);
;         if (h2) cvt_process<WT>(c, lc, scr, lane);
;     }
; }
; __global__ void __launch_bounds__(NWAVES * 64, 2) mk_fwd(Args args) {
;     ...
;             if (cb >= 128) {
;                 const bool lastl = l + 1 >= DEPTH;
;                 convert_items<true>(F.lds, wl, (const float* const*)(wl + WS_PTRS), lastl ? l : l + 1, lastl ? I_T2 : 0, lastl ? I_LAYER : I_T1, (cb - 128) * NWAVES + wave_, 128 * NWAVES, wave_, (int)(threadIdx.x & 63u));
.LBB0_549:
	s_sleep 100
	s_sleep 100
	s_lshl_b32 s4, s21, 3
	s_cmp_eq_u32 s77, 3
	s_cselect_b64 s[48:49], -1, 0
	s_and_b64 s[0:1], s[48:49], exec
	s_movk_i32 s0, 0x1d80
	s_cselect_b32 s24, s0, 0xb10
	s_movk_i32 s0, 0x1220
	s_cselect_b32 s0, s0, 0xfffffc00
	s_add_i32 s0, s0, s20
	s_add_i32 s25, s0, s4
	v_writelane_b32 v255, s77, 52
	v_mov_b32_e32 v2, v1
	s_cmp_ge_i32 s25, s24
	s_cbranch_scc1 .LBB0_736
	v_readlane_b32 s0, v255, 52
	s_add_i32 s4, s0, 1
	s_and_b64 s[0:1], s[48:49], exec
	s_cselect_b32 s0, 3, s4
	s_mul_i32 s5, s0, 0x1dc0000
	s_mul_hi_u32 s4, s0, 0x1dc0000
	s_add_u32 s12, s22, s5
	s_addc_u32 s13, s23, s4
	s_lshl_b32 s4, s20, 14
	s_add_i32 s4, s4, 0
	s_add_u32 s6, s16, 0x780078
	s_addc_u32 s7, s17, 0
	v_writelane_b32 v255, s6, 19
	s_add_u32 s56, s12, 0x1800000
	s_addc_u32 s57, s13, 0
	v_writelane_b32 v255, s7, 20
	s_mul_hi_u32 s7, s0, 0xb00000
	s_mul_i32 s6, s0, 0xb00000
	v_writelane_b32 v255, s6, 21
	s_mov_b32 s1, s37
	v_ashrrev_i32_e32 v125, 3, v2
	v_writelane_b32 v255, s7, 22
	s_add_u32 s6, s16, 0x780070
	s_addc_u32 s7, s17, 0
	s_add_u32 s62, s12, 0xd00000
	s_addc_u32 s63, s13, 0
	s_add_u32 s64, s16, 0x780060
	s_addc_u32 s65, s17, 0
	s_lshl_b32 s36, s0, 10
	s_add_u32 s66, s16, 0x780048
	s_addc_u32 s67, s17, 0
	s_lshl_b64 s[68:69], s[0:1], 22
	s_add_u32 s70, s12, 0xb00000
	s_addc_u32 s71, s13, 0
	s_add_u32 s72, s16, 0x780040
	s_addc_u32 s73, s17, 0
	s_lshl_b64 s[74:75], s[0:1], 21
	s_add_u32 s76, s12, 0x900000
	s_addc_u32 s77, s13, 0
	s_add_u32 s78, s16, 0x780038
	s_addc_u32 s79, s17, 0
	s_add_u32 s80, s16, 0x780010
	v_lshlrev_b32_e32 v4, 2, v2
	v_lshlrev_b32_e32 v2, 3, v2
	s_mul_hi_u32 s61, s0, 0x1600000
	s_mul_i32 s60, s0, 0x1600000
	s_addc_u32 s81, s17, 0
	s_mul_hi_u32 s83, s0, 0x1200000
	s_mul_i32 s82, s0, 0x1200000
	v_and_b32_e32 v4, 28, v4
	v_and_b32_e32 v124, 56, v2
	s_movk_i32 s0, 0x84
	v_writelane_b32 v255, s6, 27
	s_add_u32 s84, s16, 0x780050
	v_lshl_add_u32 v2, v4, 2, s4
	v_mul_lo_u32 v5, v125, s0
	v_mul_u32_u24_e32 v6, 0x84, v124
	v_lshlrev_b32_e32 v7, 2, v125
	v_writelane_b32 v255, s7, 28
	s_addc_u32 s85, s17, 0
	v_add_u32_e32 v132, 8, v125
	v_add_u32_e32 v133, 16, v125
	v_add_u32_e32 v134, 24, v125
	v_add3_u32 v135, s4, v6, v7
	v_lshlrev_b32_e32 v126, 2, v4
	v_lshlrev_b32_e32 v136, 2, v124
	v_add_u32_e32 v137, v2, v5
	s_branch .LBB0_554

; #define LAS __attribute__((address_space(3)))
; #define CVT_DONE() do { asm volatile("s_waitcnt vmcnt(0)" ::: "memory"); if ((threadIdx.x & 63u) == 0u) __hip_atomic_fetch_add((unsigned*)(wl + WS_CTL) + CW_CVT, 1u, __ATOMIC_RELAXED, __HIP_MEMORY_SCOPE_AGENT); } while (0)
; template <bool WT> __device__ __forceinline__ void convert_items(LAS unsigned char* lds, unsigned char* ws, const float* const* in, int l, int it0, int it1, int gw, int NGW, int wave, int lane_in) {
;     int lane = lane_in; asm volatile("" : "+v"(lane));
;     LAS float* scr = (LAS float*)(lds + RING_OFF + wave * 16384);
;     bf16* WL = (bf16*)(ws + WS_W) + (size_t)l * LAYER_W_ELEMS;
; #pragma unroll 1
;     for (int base = it0 + gw; base < it1; base += 3 * NGW) {
;         const int i1 = base + NGW, i2 = base + 2 * NGW; const bool h1 = i1 < it1, h2 = i2 < it1;
;         CvtItem a = cvt_decode(base, l, in, WL), b = cvt_decode(h1 ? i1 : base, l, in, WL), c = cvt_decode(h2 ? i2 : base, l, in, WL);
;         a.late = b.late = c.late = (!WT && l >= 1);
;         CvtLoad la, lb, lc;
;         cvt_load(a, lane, la); cvt_load(b, lane, lb); cvt_load(c, lane, lc);
; __global__ void __launch_bounds__(NWAVES * 64, 2) mk_fwd(Args args) {
;     ...
;             if (cb >= 128 && l + 1 < DEPTH) { convert_items<true>(F.lds, wl, (const float* const*)(wl + WS_PTRS), l + 1, I_T1, I_T2, (cb - 128) * NWAVES + wave_, 128 * NWAVES, wave_, (int)(threadIdx.x & 63u)); CVT_DONE(); }
.LBB0_1484:
	s_cmpk_lt_i32 s23, 0x80
	s_cselect_b64 s[0:1], -1, 0
	s_or_b64 s[0:1], s[6:7], s[0:1]
	s_and_b64 vcc, exec, s[0:1]
	s_cbranch_vccnz .LBB0_1672
	s_sleep 100
	s_sleep 100
	s_add_i32 s0, s22, s24
	s_add_i32 s1, s0, 0xfffffc00
	s_mov_b32 s39, s77
	v_mov_b32_e32 v2, v1
	s_cmpk_gt_i32 s1, 0xb0f
	s_cbranch_scc1 .LBB0_1668
	s_add_i32 s4, s39, 1
	s_mul_i32 s7, s4, 0x1dc0000
	s_mul_hi_u32 s6, s4, 0x1dc0000
	s_add_u32 s7, s10, s7
	s_addc_u32 s6, s11, s6
	s_add_u32 s12, s7, 0x800000
	s_addc_u32 s13, s6, 0
	s_add_i32 s23, s1, 0xb10
	s_lshl_b32 s1, s22, 14
	s_add_i32 s1, s1, 0
	s_add_u32 s48, s10, 0x780078
	s_mul_hi_u32 s9, s4, 0xb00000
	s_mul_i32 s8, s4, 0xb00000
	s_addc_u32 s49, s11, 0
	v_writelane_b32 v255, s8, 19
	s_mov_b32 s5, s37
	v_ashrrev_i32_e32 v125, 3, v2
	v_writelane_b32 v255, s9, 20
	s_add_u32 s8, s7, 0x2000000
	s_addc_u32 s9, s6, 0
	s_add_u32 s56, s10, 0x780070
	s_addc_u32 s57, s11, 0
	s_add_u32 s60, s7, 0x1500000
	s_addc_u32 s61, s6, 0
	s_add_u32 s62, s10, 0x780060
	s_addc_u32 s63, s11, 0
	s_lshl_b32 s36, s4, 10
	s_add_u32 s64, s10, 0x780048
	s_addc_u32 s65, s11, 0
	s_lshl_b64 s[66:67], s[4:5], 22
	s_add_u32 s68, s7, 0x1300000
	s_addc_u32 s69, s6, 0
	s_add_u32 s70, s10, 0x780040
	s_addc_u32 s71, s11, 0
	s_lshl_b64 s[72:73], s[4:5], 21
	s_add_u32 s74, s7, 0x1100000
	s_addc_u32 s75, s6, 0
	s_add_u32 s76, s10, 0x780038
	s_addc_u32 s77, s11, 0
	s_add_u32 s78, s10, 0x780010
	v_lshlrev_b32_e32 v4, 2, v2
	v_lshlrev_b32_e32 v2, 3, v2
	s_mul_hi_u32 s59, s4, 0x1600000
	s_mul_i32 s58, s4, 0x1600000
	s_addc_u32 s79, s11, 0
	s_mul_hi_u32 s81, s4, 0x1200000
	s_mul_i32 s80, s4, 0x1200000
	v_and_b32_e32 v4, 28, v4
	v_and_b32_e32 v124, 56, v2
	s_movk_i32 s4, 0x84
	v_writelane_b32 v255, s8, 21
	s_add_u32 s82, s10, 0x780050
	v_lshl_add_u32 v2, v4, 2, s1
	v_mul_lo_u32 v5, v125, s4
	v_mul_u32_u24_e32 v6, 0x84, v124
	v_lshlrev_b32_e32 v7, 2, v125
	v_writelane_b32 v255, s9, 22
	s_addc_u32 s83, s11, 0
	v_add_u32_e32 v132, 8, v125
	v_add_u32_e32 v133, 16, v125
	v_add_u32_e32 v134, 24, v125
	v_add3_u32 v135, s1, v6, v7
	s_add_i32 s22, s0, 0xfffffa10
	v_lshlrev_b32_e32 v126, 2, v4
	v_lshlrev_b32_e32 v136, 2, v124
	v_add_u32_e32 v137, v2, v5
	s_branch .LBB0_1490
